# baseline (speedup 1.0000x reference)
.Lep1_prej:
	s_waitcnt lgkmcnt(7)
	s_barrier
	s_cmp_eq_u64 s[6:7], 0
	s_cbranch_scc0 .Lep1_k1
	s_mul_i32 s43, s36, 0x5000
	s_add_i32 s43, s43, s86
	s_add_u32 s40, s18, s43
	s_addc_u32 s41, s19, 0
	v_mov_b32_e32 v18, 0
	v_mov_b32_e32 v19, 0
	v_mov_b32_e32 v20, 0
	v_mov_b32_e32 v21, 0
	ds_read2st64_b32 v[50:51], v221 offset0:0 offset1:1
	ds_read2st64_b32 v[52:53], v221 offset0:2 offset1:3
	ds_read2st64_b32 v[54:55], v221 offset0:4 offset1:5
	ds_read2st64_b32 v[56:57], v221 offset0:6 offset1:7
	ds_read2st64_b32 v[58:59], v221 offset0:8 offset1:9
	ds_read2st64_b32 v[60:61], v221 offset0:10 offset1:11
	s_waitcnt lgkmcnt(12)
	v_fma_f32 v78, -v76, v77, 0
	s_waitcnt lgkmcnt(4)
	v_pk_add_f32 v[34:35], v[34:35], v[50:51]
	v_pk_add_f32 v[36:37], v[36:37], v[52:53]
	v_pk_add_f32 v[34:35], v[34:35], v[78:79] op_sel_hi:[1,0]
	v_pk_add_f32 v[36:37], v[36:37], v[78:79] op_sel_hi:[1,0]
	v_pk_fma_f32 v[34:35], v[62:63], v[76:77], v[34:35] op_sel:[0,1,0] op_sel_hi:[1,1,1]
	v_pk_fma_f32 v[36:37], v[64:65], v[76:77], v[36:37] op_sel:[0,1,0] op_sel_hi:[1,1,1]
	v_pk_add_f32 v[18:19], v[18:19], v[34:35]
	v_pk_fma_f32 v[20:21], v[34:35], v[34:35], v[20:21]
	v_pk_add_f32 v[18:19], v[18:19], v[36:37]
	v_pk_fma_f32 v[20:21], v[36:37], v[36:37], v[20:21]
	s_waitcnt lgkmcnt(2)
	v_pk_add_f32 v[38:39], v[38:39], v[54:55]
	v_pk_add_f32 v[40:41], v[40:41], v[56:57]
	v_pk_add_f32 v[38:39], v[38:39], v[78:79] op_sel_hi:[1,0]
	v_pk_add_f32 v[40:41], v[40:41], v[78:79] op_sel_hi:[1,0]
	v_pk_fma_f32 v[38:39], v[68:69], v[76:77], v[38:39] op_sel:[0,1,0] op_sel_hi:[1,1,1]
	v_pk_fma_f32 v[40:41], v[70:71], v[76:77], v[40:41] op_sel:[0,1,0] op_sel_hi:[1,1,1]
	v_pk_add_f32 v[18:19], v[18:19], v[38:39]
	v_pk_fma_f32 v[20:21], v[38:39], v[38:39], v[20:21]
	v_pk_add_f32 v[18:19], v[18:19], v[40:41]
	v_pk_fma_f32 v[20:21], v[40:41], v[40:41], v[20:21]
	s_waitcnt lgkmcnt(0)
	v_pk_add_f32 v[42:43], v[42:43], v[58:59]
	v_pk_add_f32 v[44:45], v[44:45], v[60:61]
	v_pk_add_f32 v[42:43], v[42:43], v[78:79] op_sel_hi:[1,0]
	v_pk_add_f32 v[44:45], v[44:45], v[78:79] op_sel_hi:[1,0]
	v_pk_fma_f32 v[42:43], v[72:73], v[76:77], v[42:43] op_sel:[0,1,0] op_sel_hi:[1,1,1]
	v_pk_fma_f32 v[44:45], v[74:75], v[76:77], v[44:45] op_sel:[0,1,0] op_sel_hi:[1,1,1]
	v_pk_add_f32 v[18:19], v[18:19], v[42:43]
	v_pk_fma_f32 v[20:21], v[42:43], v[42:43], v[20:21]
	v_pk_add_f32 v[18:19], v[18:19], v[44:45]
	v_pk_fma_f32 v[20:21], v[44:45], v[44:45], v[20:21]
	ds_read2st64_b32 v[50:51], v221 offset0:12 offset1:13
	ds_read2st64_b32 v[52:53], v221 offset0:14 offset1:15
	ds_read2st64_b32 v[54:55], v221 offset0:16 offset1:17
	ds_read2st64_b32 v[56:57], v221 offset0:18 offset1:19
	ds_read2st64_b32 v[58:59], v221 offset0:20 offset1:21
	ds_read2st64_b32 v[60:61], v221 offset0:22 offset1:23
	ds_read2st64_b32 v[62:63], v67 offset0:48 offset1:50
	ds_read2st64_b32 v[64:65], v67 offset0:52 offset1:54
	ds_read2st64_b32 v[68:69], v67 offset0:64 offset1:66
	ds_read2st64_b32 v[70:71], v67 offset0:68 offset1:70
	ds_read2st64_b32 v[72:73], v67 offset0:80 offset1:82
	ds_read2st64_b32 v[74:75], v67 offset0:84 offset1:86
	s_waitcnt lgkmcnt(4)
	v_pk_add_f32 v[46:47], v[46:47], v[50:51]
	v_pk_add_f32 v[48:49], v[48:49], v[52:53]
	v_pk_add_f32 v[46:47], v[46:47], v[78:79] op_sel_hi:[1,0]
	v_pk_add_f32 v[48:49], v[48:49], v[78:79] op_sel_hi:[1,0]
	v_pk_fma_f32 v[46:47], v[62:63], v[76:77], v[46:47] op_sel:[0,1,0] op_sel_hi:[1,1,1]
	v_pk_fma_f32 v[48:49], v[64:65], v[76:77], v[48:49] op_sel:[0,1,0] op_sel_hi:[1,1,1]
	v_pk_add_f32 v[18:19], v[18:19], v[46:47]
	v_pk_fma_f32 v[20:21], v[46:47], v[46:47], v[20:21]
	v_pk_add_f32 v[18:19], v[18:19], v[48:49]
	v_pk_fma_f32 v[20:21], v[48:49], v[48:49], v[20:21]
	s_barrier
	ds_read_b32 v80, v236
	s_waitcnt lgkmcnt(3)
	v_pk_add_f32 v[2:3], v[2:3], v[54:55]
	v_pk_add_f32 v[4:5], v[4:5], v[56:57]
	v_pk_add_f32 v[2:3], v[2:3], v[78:79] op_sel_hi:[1,0]
	v_pk_add_f32 v[4:5], v[4:5], v[78:79] op_sel_hi:[1,0]
	v_pk_fma_f32 v[2:3], v[68:69], v[76:77], v[2:3] op_sel:[0,1,0] op_sel_hi:[1,1,1]
	v_pk_fma_f32 v[4:5], v[70:71], v[76:77], v[4:5] op_sel:[0,1,0] op_sel_hi:[1,1,1]
	v_pk_add_f32 v[18:19], v[18:19], v[2:3]
	v_pk_fma_f32 v[20:21], v[2:3], v[2:3], v[20:21]
	v_pk_add_f32 v[18:19], v[18:19], v[4:5]
	v_pk_fma_f32 v[20:21], v[4:5], v[4:5], v[20:21]
	s_waitcnt lgkmcnt(1)
	v_pk_add_f32 v[6:7], v[6:7], v[58:59]
	v_pk_add_f32 v[8:9], v[8:9], v[60:61]
	v_pk_add_f32 v[6:7], v[6:7], v[78:79] op_sel_hi:[1,0]
	v_pk_add_f32 v[8:9], v[8:9], v[78:79] op_sel_hi:[1,0]
	v_pk_fma_f32 v[6:7], v[72:73], v[76:77], v[6:7] op_sel:[0,1,0] op_sel_hi:[1,1,1]
	v_pk_fma_f32 v[8:9], v[74:75], v[76:77], v[8:9] op_sel:[0,1,0] op_sel_hi:[1,1,1]
	v_pk_add_f32 v[18:19], v[18:19], v[6:7]
	v_pk_fma_f32 v[20:21], v[6:7], v[6:7], v[20:21]
	v_pk_add_f32 v[18:19], v[18:19], v[8:9]
	v_pk_fma_f32 v[20:21], v[8:9], v[8:9], v[20:21]
	v_add_f32_e32 v18, v18, v19
	v_add_f32_e32 v20, v20, v21
	s_nop 1
	v_permlane32_swap_b32_e32 v18, v20
	v_add_f32_e32 v22, v18, v20
	s_branch .Lep1_wr0

.Lep2_prej:
	s_waitcnt lgkmcnt(7)
	s_barrier
	s_cmp_eq_u64 s[6:7], 0
	s_cbranch_scc0 .Lep2_k1
	s_mul_i32 s43, s36, 0x5000
	s_addk_i32 s43, 0x2800
	s_add_i32 s43, s43, s86
	s_add_u32 s40, s18, s43
	s_addc_u32 s41, s19, 0
	v_mov_b32_e32 v18, 0
	v_mov_b32_e32 v19, 0
	v_mov_b32_e32 v20, 0
	v_mov_b32_e32 v21, 0
	ds_read2st64_b32 v[50:51], v221 offset0:0 offset1:1
	ds_read2st64_b32 v[52:53], v221 offset0:2 offset1:3
	ds_read2st64_b32 v[54:55], v221 offset0:4 offset1:5
	ds_read2st64_b32 v[56:57], v221 offset0:6 offset1:7
	ds_read2st64_b32 v[58:59], v221 offset0:8 offset1:9
	ds_read2st64_b32 v[60:61], v221 offset0:10 offset1:11
	s_waitcnt lgkmcnt(12)
	v_fma_f32 v78, -v76, v77, v173
	s_waitcnt lgkmcnt(4)
	v_pk_add_f32 v[34:35], v[34:35], v[50:51]
	v_pk_add_f32 v[36:37], v[36:37], v[52:53]
	v_pk_add_f32 v[34:35], v[34:35], v[78:79] op_sel_hi:[1,0]
	v_pk_add_f32 v[36:37], v[36:37], v[78:79] op_sel_hi:[1,0]
	v_pk_fma_f32 v[34:35], v[62:63], v[76:77], v[34:35] op_sel:[0,1,0] op_sel_hi:[1,1,1]
	v_pk_fma_f32 v[36:37], v[64:65], v[76:77], v[36:37] op_sel:[0,1,0] op_sel_hi:[1,1,1]
	v_pk_add_f32 v[18:19], v[18:19], v[34:35]
	v_pk_fma_f32 v[20:21], v[34:35], v[34:35], v[20:21]
	v_pk_add_f32 v[18:19], v[18:19], v[36:37]
	v_pk_fma_f32 v[20:21], v[36:37], v[36:37], v[20:21]
	s_waitcnt lgkmcnt(2)
	v_pk_add_f32 v[38:39], v[38:39], v[54:55]
	v_pk_add_f32 v[40:41], v[40:41], v[56:57]
	v_pk_add_f32 v[38:39], v[38:39], v[78:79] op_sel_hi:[1,0]
	v_pk_add_f32 v[40:41], v[40:41], v[78:79] op_sel_hi:[1,0]
	v_pk_fma_f32 v[38:39], v[68:69], v[76:77], v[38:39] op_sel:[0,1,0] op_sel_hi:[1,1,1]
	v_pk_fma_f32 v[40:41], v[70:71], v[76:77], v[40:41] op_sel:[0,1,0] op_sel_hi:[1,1,1]
	v_pk_add_f32 v[18:19], v[18:19], v[38:39]
	v_pk_fma_f32 v[20:21], v[38:39], v[38:39], v[20:21]
	v_pk_add_f32 v[18:19], v[18:19], v[40:41]
	v_pk_fma_f32 v[20:21], v[40:41], v[40:41], v[20:21]
	s_waitcnt lgkmcnt(0)
	v_pk_add_f32 v[42:43], v[42:43], v[58:59]
	v_pk_add_f32 v[44:45], v[44:45], v[60:61]
	v_pk_add_f32 v[42:43], v[42:43], v[78:79] op_sel_hi:[1,0]
	v_pk_add_f32 v[44:45], v[44:45], v[78:79] op_sel_hi:[1,0]
	v_pk_fma_f32 v[42:43], v[72:73], v[76:77], v[42:43] op_sel:[0,1,0] op_sel_hi:[1,1,1]
	v_pk_fma_f32 v[44:45], v[74:75], v[76:77], v[44:45] op_sel:[0,1,0] op_sel_hi:[1,1,1]
	v_pk_add_f32 v[18:19], v[18:19], v[42:43]
	v_pk_fma_f32 v[20:21], v[42:43], v[42:43], v[20:21]
	v_pk_add_f32 v[18:19], v[18:19], v[44:45]
	v_pk_fma_f32 v[20:21], v[44:45], v[44:45], v[20:21]
	ds_read2st64_b32 v[50:51], v221 offset0:12 offset1:13
	ds_read2st64_b32 v[52:53], v221 offset0:14 offset1:15
	ds_read2st64_b32 v[54:55], v221 offset0:16 offset1:17
	ds_read2st64_b32 v[56:57], v221 offset0:18 offset1:19
	ds_read2st64_b32 v[58:59], v221 offset0:20 offset1:21
	ds_read2st64_b32 v[60:61], v221 offset0:22 offset1:23
	ds_read2st64_b32 v[62:63], v67 offset0:48 offset1:50
	ds_read2st64_b32 v[64:65], v67 offset0:52 offset1:54
	ds_read2st64_b32 v[68:69], v67 offset0:64 offset1:66
	ds_read2st64_b32 v[70:71], v67 offset0:68 offset1:70
	ds_read2st64_b32 v[72:73], v67 offset0:80 offset1:82
	ds_read2st64_b32 v[74:75], v67 offset0:84 offset1:86
	s_waitcnt lgkmcnt(4)
	v_pk_add_f32 v[46:47], v[46:47], v[50:51]
	v_pk_add_f32 v[48:49], v[48:49], v[52:53]
	v_pk_add_f32 v[46:47], v[46:47], v[78:79] op_sel_hi:[1,0]
	v_pk_add_f32 v[48:49], v[48:49], v[78:79] op_sel_hi:[1,0]
	v_pk_fma_f32 v[46:47], v[62:63], v[76:77], v[46:47] op_sel:[0,1,0] op_sel_hi:[1,1,1]
	v_pk_fma_f32 v[48:49], v[64:65], v[76:77], v[48:49] op_sel:[0,1,0] op_sel_hi:[1,1,1]
	v_pk_add_f32 v[18:19], v[18:19], v[46:47]
	v_pk_fma_f32 v[20:21], v[46:47], v[46:47], v[20:21]
	v_pk_add_f32 v[18:19], v[18:19], v[48:49]
	v_pk_fma_f32 v[20:21], v[48:49], v[48:49], v[20:21]
	s_barrier
	ds_read_b32 v80, v236
	s_waitcnt lgkmcnt(3)
	v_pk_add_f32 v[2:3], v[2:3], v[54:55]
	v_pk_add_f32 v[4:5], v[4:5], v[56:57]
	v_pk_add_f32 v[2:3], v[2:3], v[78:79] op_sel_hi:[1,0]
	v_pk_add_f32 v[4:5], v[4:5], v[78:79] op_sel_hi:[1,0]
	v_pk_fma_f32 v[2:3], v[68:69], v[76:77], v[2:3] op_sel:[0,1,0] op_sel_hi:[1,1,1]
	v_pk_fma_f32 v[4:5], v[70:71], v[76:77], v[4:5] op_sel:[0,1,0] op_sel_hi:[1,1,1]
	v_pk_add_f32 v[18:19], v[18:19], v[2:3]
	v_pk_fma_f32 v[20:21], v[2:3], v[2:3], v[20:21]
	v_pk_add_f32 v[18:19], v[18:19], v[4:5]
	v_pk_fma_f32 v[20:21], v[4:5], v[4:5], v[20:21]
	s_waitcnt lgkmcnt(1)
	v_pk_add_f32 v[6:7], v[6:7], v[58:59]
	v_pk_add_f32 v[8:9], v[8:9], v[60:61]
	v_pk_add_f32 v[6:7], v[6:7], v[78:79] op_sel_hi:[1,0]
	v_pk_add_f32 v[8:9], v[8:9], v[78:79] op_sel_hi:[1,0]
	v_pk_fma_f32 v[6:7], v[72:73], v[76:77], v[6:7] op_sel:[0,1,0] op_sel_hi:[1,1,1]
	v_pk_fma_f32 v[8:9], v[74:75], v[76:77], v[8:9] op_sel:[0,1,0] op_sel_hi:[1,1,1]
	v_pk_add_f32 v[18:19], v[18:19], v[6:7]
	v_pk_fma_f32 v[20:21], v[6:7], v[6:7], v[20:21]
	v_pk_add_f32 v[18:19], v[18:19], v[8:9]
	v_pk_fma_f32 v[20:21], v[8:9], v[8:9], v[20:21]
	v_add_f32_e32 v18, v18, v19
	v_add_f32_e32 v20, v20, v21
	s_nop 1
	v_permlane32_swap_b32_e32 v18, v20
	v_add_f32_e32 v22, v18, v20
	s_branch .Lep2_wr0

.LBB1_207:
	s_or_b64 exec, exec, s[40:41]
	s_andn2_b64 vcc, exec, s[30:31]
	s_mov_b64 s[2:3], -1
	v_mov_b32_e32 v54, v0
	v_and_b32_e32 v56, 31, v54
	v_lshlrev_b32_e32 v46, 4, v56
	v_add_u32_e32 v47, 0x25680, v46
	v_add_u32_e32 v46, 0x25880, v46
	v_ashrrev_i32_e32 v55, 5, v54
	v_lshlrev_b32_e32 v54, 3, v56
	v_mad_u32_u24 v56, v55, s64, v54
	s_waitcnt lgkmcnt(0)
	s_barrier
	s_cbranch_vccnz .LBB1_221
	s_nop 0
	ds_read_b128 v[50:53], v47
	ds_read_b128 v[46:49], v46
	s_waitcnt lgkmcnt(0)
	v_pk_mul_f32 v[50:51], v[50:51], v[46:47] neg_lo:[1,0] neg_hi:[1,0]
	v_pk_mul_f32 v[52:53], v[52:53], v[48:49] neg_lo:[1,0] neg_hi:[1,0]
	v_pk_fma_f32 v[42:43], v[42:43], v[46:47], v[50:51]
	v_pk_fma_f32 v[44:45], v[44:45], v[48:49], v[52:53]
	v_pk_fma_f32 v[38:39], v[38:39], v[46:47], v[50:51]
	v_pk_fma_f32 v[40:41], v[40:41], v[48:49], v[52:53]
	v_pk_fma_f32 v[34:35], v[34:35], v[46:47], v[50:51]
	v_pk_fma_f32 v[36:37], v[36:37], v[48:49], v[52:53]
	v_pk_fma_f32 v[30:31], v[30:31], v[46:47], v[50:51]
	v_pk_fma_f32 v[32:33], v[32:33], v[48:49], v[52:53]
	v_pk_fma_f32 v[22:23], v[22:23], v[46:47], v[50:51]
	v_pk_fma_f32 v[24:25], v[24:25], v[48:49], v[52:53]
	v_cvt_pk_f16_f32 v42, v42, v43
	v_cvt_pk_f16_f32 v43, v44, v45
	ds_write_b64 v56, v[42:43] offset:43008
	v_cvt_pk_f16_f32 v38, v38, v39
	v_cvt_pk_f16_f32 v39, v40, v41
	ds_write_b64 v56, v[38:39] offset:47360
	v_cvt_pk_f16_f32 v34, v34, v35
	v_cvt_pk_f16_f32 v35, v36, v37
	ds_write_b64 v56, v[34:35] offset:51712
	v_cvt_pk_f16_f32 v30, v30, v31
	v_cvt_pk_f16_f32 v31, v32, v33
	ds_write_b64 v56, v[30:31] offset:56064
	v_cvt_pk_f16_f32 v22, v22, v23
	v_cvt_pk_f16_f32 v23, v24, v25
	ds_write_b64 v56, v[22:23] offset:60416
	v_cmp_gt_i32_e32 vcc, 4, v55
	s_and_saveexec_b64 s[2:3], vcc
	v_pk_fma_f32 v[18:19], v[18:19], v[46:47], v[50:51]
	v_pk_fma_f32 v[20:21], v[20:21], v[48:49], v[52:53]
	v_cvt_pk_f16_f32 v18, v18, v19
	v_cvt_pk_f16_f32 v19, v20, v21
	ds_write_b64 v56, v[18:19] offset:64768
	s_or_b64 exec, exec, s[2:3]
	s_mov_b64 s[2:3], 0
	s_waitcnt lgkmcnt(0)
	s_barrier
